# P3 gated-merge epilogue: 16 gate pieces loaded together (counted vmcnt) ; cvt_wg x32 scale as in-place v_pk_mul_f32
# speedup vs baseline: 1.0056x; 1.0056x over previous
.LBB0_538:
	s_mov_b32 s98, 0x42000000
	s_mov_b32 s99, 0x42000000
	v_readlane_b32 s4, v254, 7
	s_cmp_lt_i32 s4, 3
	v_readlane_b32 s5, v254, 8
	s_cselect_b64 s[2:3], -1, 0
	s_add_u32 s4, s92, 0x3dc00000
	s_addc_u32 s5, s93, 0
	v_readlane_b32 s6, v254, 9
	v_readlane_b32 s7, v254, 10
	v_writelane_b32 v254, s4, 51
	s_nop 1
	v_writelane_b32 v254, s5, 52
	s_and_b64 s[4:5], s[2:3], s[0:1]
	v_writelane_b32 v254, s82, 53
	s_andn2_b64 vcc, exec, s[4:5]
	s_nop 0
	v_writelane_b32 v254, s83, 54
	s_cbranch_vccnz .LBB0_836
	v_writelane_b32 v254, s4, 55
	s_add_u32 s46, s92, 0x3d900000
	s_addc_u32 s47, s93, 0
	v_writelane_b32 v254, s5, 56
	s_and_b32 s81, s90, 7
	v_readlane_b32 s82, v254, 51
	v_readfirstlane_b32 s2, v0
	v_and_b32_e32 v181, 15, v0
	s_cmp_gt_i32 s90, 15
	v_lshlrev_b32_e32 v142, 2, v0
	v_readlane_b32 s83, v254, 52
	s_cbranch_scc1 .LBB0_550
	v_lshrrev_b32_e32 v1, 5, v0
	s_waitcnt vmcnt(0)
	v_lshrrev_b32_e32 v3, 1, v0
	v_and_b32_e32 v1, 4, v1
	v_bfe_u32 v2, v0, 2, 2
	v_and_b32_e32 v143, 24, v3
	v_bfe_u32 v3, v0, 3, 25
	v_or3_b32 v1, v1, v2, v143
	v_or_b32_e32 v4, 64, v3
	s_movk_i32 s0, 0x60
	v_and_or_b32 v3, v4, s0, v1
	v_lshlrev_b32_e32 v2, 4, v0
	v_mul_u32_u24_e32 v5, 0x840, v3
	v_and_b32_e32 v3, 32, v0
	v_bitop3_b32 v2, v2, v3, 48 bitop3:0x6c
	v_and_b32_e32 v3, 64, v0
	v_or_b32_e32 v6, v2, v3
	v_lshrrev_b32_e32 v6, 1, v6
	v_or_b32_e32 v5, v5, v6
	v_lshlrev_b32_e32 v130, 1, v5
	v_bfe_u32 v5, v0, 2, 4
	s_movk_i32 s0, 0x70
	v_and_or_b32 v4, v4, s0, v5
	v_mul_u32_u24_e32 v4, 0x840, v4
	v_or_b32_e32 v7, v4, v6
	v_lshlrev_b32_e32 v132, 1, v7
	v_lshrrev_b32_e32 v7, 3, v0
	v_and_or_b32 v1, v7, 32, v1
	v_mul_u32_u24_e32 v1, 0x840, v1
	s_lshr_b32 s14, s2, 6
	v_or_b32_e32 v1, v1, v6
	s_lshr_b32 s15, s2, 8
	s_lshl_b32 s18, s14, 10
	s_ashr_i32 s3, s90, 3
	v_lshlrev_b32_e32 v134, 1, v1
	v_and_or_b32 v1, v7, 48, v5
	s_mul_i32 s16, s81, 0x108000
	v_mul_u32_u24_e32 v5, 0x840, v1
	s_add_u32 s0, s38, s16
	v_or_b32_e32 v1, v6, v5
	s_addc_u32 s1, s39, 0
	s_add_i32 s22, s18, 0
	v_lshlrev_b32_e32 v136, 1, v1
	v_mov_b32_e32 v1, 0
	v_mov_b32_e32 v6, 0
	s_add_i32 m0, s22, 0x10000
	s_mul_i32 s19, s3, 0x108000
	global_load_lds_dwordx4 v134, s[0:1]
	s_add_i32 m0, s22, 0x12000
	s_add_u32 s4, s0, 0x84000
	global_load_lds_dwordx4 v130, s[0:1]
	s_addc_u32 s5, s1, 0
	s_add_i32 m0, s22, 0x14000
	s_mul_hi_i32 s17, s3, 0x108000
	global_load_lds_dwordx4 v134, s[4:5]
	s_add_i32 m0, s22, 0x16000
	s_add_u32 s6, s92, s19
	s_addc_u32 s7, s93, s17
	global_load_lds_dwordx4 v130, s[4:5]
	s_add_u32 s4, s6, 0x23300000
	s_addc_u32 s5, s7, 0
	s_add_i32 s23, s22, 0x2000
	s_mov_b32 m0, s22
	s_add_u32 s6, s6, 0x23384000
	global_load_lds_dwordx4 v136, s[4:5]
	s_mov_b32 m0, s23
	s_addc_u32 s7, s7, 0
	s_add_i32 s24, s22, 0x4000
	global_load_lds_dwordx4 v132, s[4:5]
	s_mov_b32 m0, s24
	s_add_i32 s25, s22, 0x6000
	v_mov_b32_e32 v135, 0
	global_load_lds_dwordx4 v136, s[6:7]
	s_mov_b32 m0, s25
	v_lshl_add_u64 v[6:7], s[0:1], 0, v[134:135]
	v_mov_b32_e32 v131, v135
	global_load_lds_dwordx4 v132, s[6:7]
	s_mov_b64 s[6:7], 0x80
	v_lshl_add_u64 v[8:9], s[0:1], 0, v[130:131]
	v_mov_b32_e32 v137, v135
	s_add_i32 m0, s22, 0x18000
	v_lshl_add_u64 v[6:7], v[6:7], 0, s[6:7]
	v_lshl_add_u64 v[10:11], s[4:5], 0, v[136:137]
	v_mov_b32_e32 v133, v135
	global_load_lds_dwordx4 v[6:7], off
	v_lshl_add_u64 v[6:7], v[8:9], 0, s[6:7]
	s_add_i32 m0, s22, 0x1a000
	s_add_i32 s26, s22, 0x8000
	v_lshl_add_u64 v[12:13], s[4:5], 0, v[132:133]
	global_load_lds_dwordx4 v[6:7], off
	v_lshl_add_u64 v[6:7], v[10:11], 0, s[6:7]
	s_mov_b32 m0, s26
	s_add_i32 s27, s22, 0xa000
	global_load_lds_dwordx4 v[6:7], off
	v_lshl_add_u64 v[6:7], v[12:13], 0, s[6:7]
	s_mov_b32 m0, s27
	s_add_u32 s20, s0, 0x84080
	global_load_lds_dwordx4 v[6:7], off
	s_addc_u32 s21, s1, 0
	s_add_i32 m0, s22, 0x1c000
	s_nop 0
	global_load_lds_dwordx4 v134, s[20:21]
	s_add_i32 m0, s22, 0x1e000
	s_cmp_lg_u32 s15, 1
	global_load_lds_dwordx4 v130, s[20:21]
	s_cbranch_scc1 .LBB0_542
	s_barrier

.LBB0_600:
	s_waitcnt vmcnt(7)
	v_pk_mul_f32 v[4:5], v[4:5], s[98:99]
	s_waitcnt vmcnt(30)
	v_pk_mul_f32 v[8:9], v[8:9], s[98:99]
	v_cvt_pk_fp8_f32 v1, v4, v8
	s_waitcnt vmcnt(29)
	v_pk_mul_f32 v[12:13], v[12:13], s[98:99]
	s_waitcnt vmcnt(5)
	v_pk_mul_f32 v[16:17], v[16:17], s[98:99]
	v_cvt_pk_fp8_f32 v1, v12, v16 op_sel:[0,0,1]
	v_cvt_pk_fp8_f32 v132, v5, v9
	v_pk_mul_f32 v[14:15], v[14:15], s[98:99]
	v_cvt_pk_fp8_f32 v132, v13, v17 op_sel:[0,0,1]
	v_pk_mul_f32 v[18:19], v[18:19], s[98:99]
	s_waitcnt vmcnt(2)
	v_pk_mul_f32 v[34:35], v[34:35], s[98:99]
	ds_write2_b32 v195, v1, v132 offset1:33
	v_pk_mul_f32 v[6:7], v[6:7], s[98:99]
	v_pk_mul_f32 v[10:11], v[10:11], s[98:99]
	v_cvt_pk_fp8_f32 v1, v6, v10
	s_add_i32 s28, s5, 4
	s_cmp_ge_u32 s28, s69
	v_cvt_pk_fp8_f32 v1, v14, v18 op_sel:[0,0,1]
	v_cvt_pk_fp8_f32 v132, v7, v11
	v_pk_mul_f32 v[28:29], v[28:29], s[98:99]
	s_cselect_b64 s[16:17], -1, 0
	v_cvt_pk_fp8_f32 v132, v15, v19 op_sel:[0,0,1]
	v_pk_mul_f32 v[32:33], v[32:33], s[98:99]
	s_and_b64 vcc, exec, s[16:17]
	ds_write2_b32 v195, v1, v132 offset0:66 offset1:99
	v_pk_mul_f32 v[20:21], v[20:21], s[98:99]
	v_pk_mul_f32 v[24:25], v[24:25], s[98:99]
	v_cvt_pk_fp8_f32 v1, v20, v24
	v_cvt_pk_fp8_f32 v1, v28, v32 op_sel:[0,0,1]
	v_cvt_pk_fp8_f32 v132, v21, v25
	v_pk_mul_f32 v[30:31], v[30:31], s[98:99]
	v_cvt_pk_fp8_f32 v132, v29, v33 op_sel:[0,0,1]
	v_add_u32_e32 v134, 0x2000, v195
	ds_write2_b32 v134, v1, v132 offset0:64 offset1:97
	v_pk_mul_f32 v[22:23], v[22:23], s[98:99]
	v_pk_mul_f32 v[26:27], v[26:27], s[98:99]
	v_cvt_pk_fp8_f32 v1, v22, v26
	v_cvt_pk_fp8_f32 v1, v30, v34 op_sel:[0,0,1]
	v_cvt_pk_fp8_f32 v132, v23, v27
	v_cvt_pk_fp8_f32 v132, v31, v35 op_sel:[0,0,1]
	ds_write2_b32 v134, v1, v132 offset0:130 offset1:163
	s_cbranch_vccnz .LBB0_607
	s_add_i32 s27, s8, s5
	s_add_i32 s26, s27, 4
	s_cmpk_gt_i32 s26, 0x3fff
	s_mov_b64 s[24:25], -1
	s_cbranch_scc0 .LBB0_603
	s_addk_i32 s27, 0xc004
	s_lshr_b32 s42, s27, 8
	s_add_i32 s14, s2, 32
	s_add_i32 s15, s4, 0x200
	v_readlane_b32 s52, v254, 31
	s_and_b32 s14, s14, 0x780
	s_and_b32 s24, s15, 0x600
	s_lshl_b64 s[22:23], s[42:43], 11
	s_lshl_b64 s[20:21], s[42:43], 24
	v_readlane_b32 s64, v254, 43
	v_readlane_b32 s65, v254, 44
	s_add_u32 s20, s64, s20
	s_addc_u32 s21, s65, s21
	s_lshl_b32 s25, s14, 13
	s_add_u32 s20, s20, s25
	s_addc_u32 s21, s21, 0
	s_lshl_b32 s25, s24, 2
	s_add_u32 s20, s20, s25
	v_readlane_b32 s53, v254, 32
	v_readlane_b32 s54, v254, 33
	v_readlane_b32 s55, v254, 34
	v_readlane_b32 s56, v254, 35
	v_readlane_b32 s57, v254, 36
	v_readlane_b32 s58, v254, 37
	v_readlane_b32 s59, v254, 38
	v_readlane_b32 s60, v254, 39
	v_readlane_b32 s61, v254, 40
	v_readlane_b32 s62, v254, 41
	v_readlane_b32 s63, v254, 42
	v_readlane_b32 s66, v254, 45
	v_readlane_b32 s67, v254, 46
	s_mov_b32 s15, s43
	s_addc_u32 s21, s21, 0
	s_or_b32 s22, s22, s24
	s_mov_b64 s[24:25], 0

.LBB0_610:
	s_waitcnt vmcnt(25)
	v_pk_mul_f32 v[36:37], v[36:37], s[98:99]
	s_waitcnt vmcnt(24)
	v_pk_mul_f32 v[40:41], v[40:41], s[98:99]
	v_cvt_pk_fp8_f32 v1, v36, v40
	s_waitcnt vmcnt(23)
	v_pk_mul_f32 v[44:45], v[44:45], s[98:99]
	s_waitcnt vmcnt(22)
	v_pk_mul_f32 v[52:53], v[52:53], s[98:99]
	v_cvt_pk_fp8_f32 v1, v44, v52 op_sel:[0,0,1]
	v_cvt_pk_fp8_f32 v135, v37, v41
	v_add_u32_e32 v136, 0x4000, v195
	v_cvt_pk_fp8_f32 v135, v45, v53 op_sel:[0,0,1]
	v_pk_mul_f32 v[46:47], v[46:47], s[98:99]
	v_pk_mul_f32 v[54:55], v[54:55], s[98:99]
	ds_write2_b32 v136, v1, v135 offset0:128 offset1:161
	v_pk_mul_f32 v[38:39], v[38:39], s[98:99]
	v_pk_mul_f32 v[42:43], v[42:43], s[98:99]
	v_cvt_pk_fp8_f32 v1, v38, v42
	s_add_i32 s18, s5, 5
	s_cmp_ge_u32 s18, s69
	v_cvt_pk_fp8_f32 v1, v46, v54 op_sel:[0,0,1]
	v_cvt_pk_fp8_f32 v135, v39, v43
	s_waitcnt vmcnt(18)
	v_pk_mul_f32 v[64:65], v[64:65], s[98:99]
	s_mov_b64 s[18:19], s[10:11]
	v_cvt_pk_fp8_f32 v135, v47, v55 op_sel:[0,0,1]
	ds_write2_b32 v136, v1, v135 offset0:194 offset1:227
	v_pk_mul_f32 v[48:49], v[48:49], s[98:99]
	v_pk_mul_f32 v[56:57], v[56:57], s[98:99]
	v_cvt_pk_fp8_f32 v1, v48, v56
	v_pk_mul_f32 v[60:61], v[60:61], s[98:99]
	v_cvt_pk_fp8_f32 v1, v60, v64 op_sel:[0,0,1]
	v_cvt_pk_fp8_f32 v135, v49, v57
	v_add_u32_e32 v136, 0x6000, v195
	v_cvt_pk_fp8_f32 v135, v61, v65 op_sel:[0,0,1]
	v_pk_mul_f32 v[66:67], v[66:67], s[98:99]
	ds_write2_b32 v136, v1, v135 offset0:192 offset1:225
	v_pk_mul_f32 v[50:51], v[50:51], s[98:99]
	v_pk_mul_f32 v[58:59], v[58:59], s[98:99]
	v_cvt_pk_fp8_f32 v1, v50, v58
	v_pk_mul_f32 v[62:63], v[62:63], s[98:99]
	v_cvt_pk_fp8_f32 v1, v62, v66 op_sel:[0,0,1]
	v_cvt_pk_fp8_f32 v135, v51, v59
	v_add_u32_e32 v136, 0x6400, v195
	v_cvt_pk_fp8_f32 v135, v63, v67 op_sel:[0,0,1]
	ds_write2_b32 v136, v1, v135 offset0:2 offset1:35
	s_cbranch_scc1 .LBB0_617
	s_add_i32 s27, s8, s5
	s_add_i32 s26, s27, 5
	s_cmpk_gt_i32 s26, 0x3fff
	s_mov_b64 s[24:25], -1
	s_cbranch_scc0 .LBB0_613
	s_addk_i32 s27, 0xc005
	s_lshr_b32 s42, s27, 8
	s_add_i32 s18, s2, 40
	s_add_i32 s19, s4, 0x280
	v_readlane_b32 s52, v254, 31
	s_and_b32 s18, s18, 0x780
	s_and_b32 s24, s19, 0x680
	s_lshl_b64 s[22:23], s[42:43], 11
	s_lshl_b64 s[20:21], s[42:43], 24
	v_readlane_b32 s64, v254, 43
	v_readlane_b32 s65, v254, 44
	s_add_u32 s20, s64, s20
	s_addc_u32 s21, s65, s21
	s_lshl_b32 s25, s18, 13
	s_add_u32 s20, s20, s25
	s_addc_u32 s21, s21, 0
	s_lshl_b32 s25, s24, 2
	s_add_u32 s20, s20, s25
	v_readlane_b32 s53, v254, 32
	v_readlane_b32 s54, v254, 33
	v_readlane_b32 s55, v254, 34
	v_readlane_b32 s56, v254, 35
	v_readlane_b32 s57, v254, 36
	v_readlane_b32 s58, v254, 37
	v_readlane_b32 s59, v254, 38
	v_readlane_b32 s60, v254, 39
	v_readlane_b32 s61, v254, 40
	v_readlane_b32 s62, v254, 41
	v_readlane_b32 s63, v254, 42
	v_readlane_b32 s66, v254, 45
	v_readlane_b32 s67, v254, 46
	s_mov_b32 s19, s43
	s_addc_u32 s21, s21, 0
	s_or_b32 s22, s22, s24
	s_mov_b64 s[24:25], 0

.LBB0_618:
	s_waitcnt vmcnt(17)
	v_pk_mul_f32 v[68:69], v[68:69], s[98:99]
	s_waitcnt vmcnt(16)
	v_pk_mul_f32 v[72:73], v[72:73], s[98:99]
	v_cvt_pk_fp8_f32 v1, v68, v72
	s_waitcnt vmcnt(15)
	v_pk_mul_f32 v[76:77], v[76:77], s[98:99]
	s_waitcnt vmcnt(14)
	v_pk_mul_f32 v[84:85], v[84:85], s[98:99]
	v_cvt_pk_fp8_f32 v1, v76, v84 op_sel:[0,0,1]
	v_cvt_pk_fp8_f32 v135, v69, v73
	v_pk_mul_f32 v[78:79], v[78:79], s[98:99]
	v_cvt_pk_fp8_f32 v135, v77, v85 op_sel:[0,0,1]
	v_pk_mul_f32 v[86:87], v[86:87], s[98:99]
	s_add_i32 s18, s5, 6
	ds_write2_b32 v195, v1, v135 offset1:33
	v_pk_mul_f32 v[70:71], v[70:71], s[98:99]
	v_pk_mul_f32 v[74:75], v[74:75], s[98:99]
	v_cvt_pk_fp8_f32 v1, v70, v74
	s_cmp_ge_u32 s18, s69
	s_mov_b64 s[18:19], s[0:1]
	v_cvt_pk_fp8_f32 v1, v78, v86 op_sel:[0,0,1]
	v_cvt_pk_fp8_f32 v135, v71, v75
	s_waitcnt vmcnt(11)
	v_pk_mul_f32 v[92:93], v[92:93], s[98:99]
	v_cvt_pk_fp8_f32 v135, v79, v87 op_sel:[0,0,1]
	s_waitcnt vmcnt(10)
	v_pk_mul_f32 v[96:97], v[96:97], s[98:99]
	ds_write2_b32 v195, v1, v135 offset0:66 offset1:99
	v_pk_mul_f32 v[80:81], v[80:81], s[98:99]
	v_pk_mul_f32 v[88:89], v[88:89], s[98:99]
	v_cvt_pk_fp8_f32 v1, v80, v88
	v_cvt_pk_fp8_f32 v1, v92, v96 op_sel:[0,0,1]
	v_cvt_pk_fp8_f32 v135, v81, v89
	v_pk_mul_f32 v[94:95], v[94:95], s[98:99]
	v_cvt_pk_fp8_f32 v135, v93, v97 op_sel:[0,0,1]
	v_pk_mul_f32 v[98:99], v[98:99], s[98:99]
	ds_write2_b32 v134, v1, v135 offset0:64 offset1:97
	v_pk_mul_f32 v[82:83], v[82:83], s[98:99]
	v_pk_mul_f32 v[90:91], v[90:91], s[98:99]
	v_cvt_pk_fp8_f32 v1, v82, v90
	v_cvt_pk_fp8_f32 v1, v94, v98 op_sel:[0,0,1]
	v_cvt_pk_fp8_f32 v135, v83, v91
	v_cvt_pk_fp8_f32 v135, v95, v99 op_sel:[0,0,1]
	ds_write2_b32 v134, v1, v135 offset0:130 offset1:163
	s_cbranch_scc1 .LBB0_625
	s_add_i32 s27, s8, s5
	s_add_i32 s26, s27, 6
	s_cmpk_gt_i32 s26, 0x3fff
	s_mov_b64 s[24:25], -1
	s_cbranch_scc0 .LBB0_621
	s_addk_i32 s27, 0xc006
	s_lshr_b32 s42, s27, 8
	s_add_i32 s18, s2, 48
	s_add_i32 s19, s4, 0x300
	v_readlane_b32 s52, v254, 31
	s_and_b32 s18, s18, 0x780
	s_and_b32 s24, s19, 0x700
	s_lshl_b64 s[22:23], s[42:43], 11
	s_lshl_b64 s[20:21], s[42:43], 24
	v_readlane_b32 s64, v254, 43
	v_readlane_b32 s65, v254, 44
	s_add_u32 s20, s64, s20
	s_addc_u32 s21, s65, s21
	s_lshl_b32 s25, s18, 13
	s_add_u32 s20, s20, s25
	s_addc_u32 s21, s21, 0
	s_lshl_b32 s25, s24, 2
	s_add_u32 s20, s20, s25
	v_readlane_b32 s53, v254, 32
	v_readlane_b32 s54, v254, 33
	v_readlane_b32 s55, v254, 34
	v_readlane_b32 s56, v254, 35
	v_readlane_b32 s57, v254, 36
	v_readlane_b32 s58, v254, 37
	v_readlane_b32 s59, v254, 38
	v_readlane_b32 s60, v254, 39
	v_readlane_b32 s61, v254, 40
	v_readlane_b32 s62, v254, 41
	v_readlane_b32 s63, v254, 42
	v_readlane_b32 s66, v254, 45
	v_readlane_b32 s67, v254, 46
	s_mov_b32 s19, s43
	s_addc_u32 s21, s21, 0
	s_or_b32 s22, s22, s24
	s_mov_b64 s[24:25], 0

.LBB0_626:
	s_waitcnt vmcnt(7)
	v_pk_mul_f32 v[108:109], v[108:109], s[98:99]
	v_pk_mul_f32 v[100:101], v[100:101], s[98:99]
	v_cvt_pk_fp8_f32 v1, v108, v100
	v_pk_mul_f32 v[104:105], v[104:105], s[98:99]
	s_waitcnt vmcnt(5)
	v_pk_mul_f32 v[116:117], v[116:117], s[98:99]
	v_cvt_pk_fp8_f32 v1, v104, v116 op_sel:[0,0,1]
	v_cvt_pk_fp8_f32 v134, v109, v101
	v_add_u32_e32 v135, 0x4000, v195
	v_cvt_pk_fp8_f32 v134, v105, v117 op_sel:[0,0,1]
	v_pk_mul_f32 v[106:107], v[106:107], s[98:99]
	v_pk_mul_f32 v[118:119], v[118:119], s[98:99]
	ds_write2_b32 v135, v1, v134 offset0:128 offset1:161
	v_pk_mul_f32 v[110:111], v[110:111], s[98:99]
	v_pk_mul_f32 v[102:103], v[102:103], s[98:99]
	v_cvt_pk_fp8_f32 v1, v110, v102
	s_add_i32 s18, s5, 7
	s_cmp_ge_u32 s18, s69
	v_cvt_pk_fp8_f32 v1, v106, v118 op_sel:[0,0,1]
	v_cvt_pk_fp8_f32 v134, v111, v103
	s_waitcnt vmcnt(2)
	v_pk_mul_f32 v[128:129], v[128:129], s[98:99]
	s_mov_b64 s[18:19], s[12:13]
	v_cvt_pk_fp8_f32 v134, v107, v119 op_sel:[0,0,1]
	ds_write2_b32 v135, v1, v134 offset0:194 offset1:227
	v_pk_mul_f32 v[112:113], v[112:113], s[98:99]
	v_pk_mul_f32 v[120:121], v[120:121], s[98:99]
	v_cvt_pk_fp8_f32 v1, v112, v120
	v_pk_mul_f32 v[124:125], v[124:125], s[98:99]
	v_cvt_pk_fp8_f32 v1, v124, v128 op_sel:[0,0,1]
	v_cvt_pk_fp8_f32 v134, v113, v121
	v_add_u32_e32 v135, 0x6000, v195
	v_cvt_pk_fp8_f32 v134, v125, v129 op_sel:[0,0,1]
	v_pk_mul_f32 v[130:131], v[130:131], s[98:99]
	ds_write2_b32 v135, v1, v134 offset0:192 offset1:225
	v_pk_mul_f32 v[114:115], v[114:115], s[98:99]
	v_pk_mul_f32 v[122:123], v[122:123], s[98:99]
	v_cvt_pk_fp8_f32 v1, v114, v122
	v_pk_mul_f32 v[126:127], v[126:127], s[98:99]
	v_cvt_pk_fp8_f32 v1, v126, v130 op_sel:[0,0,1]
	v_cvt_pk_fp8_f32 v134, v115, v123
	v_add_u32_e32 v135, 0x6400, v195
	v_cvt_pk_fp8_f32 v134, v127, v131 op_sel:[0,0,1]
	ds_write2_b32 v135, v1, v134 offset0:2 offset1:35
	s_cbranch_scc1 .LBB0_598
	s_add_i32 s26, s8, s5
	s_add_i32 s5, s26, 7
	s_cmpk_gt_i32 s5, 0x3fff
	s_mov_b64 s[24:25], -1
	s_cbranch_scc0 .LBB0_629
	s_addk_i32 s26, 0xc007
	s_lshr_b32 s42, s26, 8
	s_add_i32 s18, s2, 56
	s_add_i32 s19, s4, 0x380
	v_readlane_b32 s52, v254, 31
	s_and_b32 s18, s18, 0x780
	s_and_b32 s24, s19, 0x780
	s_lshl_b64 s[22:23], s[42:43], 11
	s_lshl_b64 s[20:21], s[42:43], 24
	v_readlane_b32 s64, v254, 43
	v_readlane_b32 s65, v254, 44
	s_add_u32 s20, s64, s20
	s_addc_u32 s21, s65, s21
	s_lshl_b32 s25, s18, 13
	s_add_u32 s20, s20, s25
	s_addc_u32 s21, s21, 0
	s_lshl_b32 s25, s24, 2
	s_add_u32 s20, s20, s25
	v_readlane_b32 s53, v254, 32
	v_readlane_b32 s54, v254, 33
	v_readlane_b32 s55, v254, 34
	v_readlane_b32 s56, v254, 35
	v_readlane_b32 s57, v254, 36
	v_readlane_b32 s58, v254, 37
	v_readlane_b32 s59, v254, 38
	v_readlane_b32 s60, v254, 39
	v_readlane_b32 s61, v254, 40
	v_readlane_b32 s62, v254, 41
	v_readlane_b32 s63, v254, 42
	v_readlane_b32 s66, v254, 45
	v_readlane_b32 s67, v254, 46
	s_mov_b32 s19, s43
	s_addc_u32 s21, s21, 0
	s_or_b32 s22, s22, s24
	s_mov_b64 s[24:25], 0

.LBB0_754:
	s_waitcnt vmcnt(7)
	v_pk_mul_f32 v[12:13], v[12:13], s[98:99]
	v_pk_mul_f32 v[4:5], v[4:5], s[98:99]
	v_cvt_pk_fp8_f32 v1, v12, v4
	v_pk_mul_f32 v[8:9], v[8:9], s[98:99]
	s_waitcnt vmcnt(5)
	v_pk_mul_f32 v[20:21], v[20:21], s[98:99]
	v_cvt_pk_fp8_f32 v1, v8, v20 op_sel:[0,0,1]
	v_cvt_pk_fp8_f32 v132, v13, v5
	v_pk_mul_f32 v[10:11], v[10:11], s[98:99]
	v_cvt_pk_fp8_f32 v132, v9, v21 op_sel:[0,0,1]
	v_pk_mul_f32 v[22:23], v[22:23], s[98:99]
	s_waitcnt vmcnt(2)
	v_pk_mul_f32 v[34:35], v[34:35], s[98:99]
	ds_write2_b32 v195, v1, v132 offset1:33
	v_pk_mul_f32 v[14:15], v[14:15], s[98:99]
	v_pk_mul_f32 v[6:7], v[6:7], s[98:99]
	v_cvt_pk_fp8_f32 v1, v14, v6
	s_add_i32 s9, s5, 4
	s_cmp_ge_u32 s9, s71
	v_cvt_pk_fp8_f32 v1, v10, v22 op_sel:[0,0,1]
	v_cvt_pk_fp8_f32 v132, v15, v7
	v_pk_mul_f32 v[28:29], v[28:29], s[98:99]
	s_cselect_b64 s[16:17], -1, 0
	v_cvt_pk_fp8_f32 v132, v11, v23 op_sel:[0,0,1]
	v_pk_mul_f32 v[32:33], v[32:33], s[98:99]
	s_and_b64 vcc, exec, s[16:17]
	ds_write2_b32 v195, v1, v132 offset0:66 offset1:99
	v_pk_mul_f32 v[16:17], v[16:17], s[98:99]
	v_pk_mul_f32 v[24:25], v[24:25], s[98:99]
	v_cvt_pk_fp8_f32 v1, v16, v24
	v_cvt_pk_fp8_f32 v1, v28, v32 op_sel:[0,0,1]
	v_cvt_pk_fp8_f32 v132, v17, v25
	v_pk_mul_f32 v[30:31], v[30:31], s[98:99]
	v_cvt_pk_fp8_f32 v132, v29, v33 op_sel:[0,0,1]
	v_add_u32_e32 v134, 0x2000, v195
	ds_write2_b32 v134, v1, v132 offset0:64 offset1:97
	v_pk_mul_f32 v[18:19], v[18:19], s[98:99]
	v_pk_mul_f32 v[26:27], v[26:27], s[98:99]
	v_cvt_pk_fp8_f32 v1, v18, v26
	v_cvt_pk_fp8_f32 v1, v30, v34 op_sel:[0,0,1]
	v_cvt_pk_fp8_f32 v132, v19, v27
	v_cvt_pk_fp8_f32 v132, v31, v35 op_sel:[0,0,1]
	ds_write2_b32 v134, v1, v132 offset0:130 offset1:163
	s_cbranch_vccnz .LBB0_761
	s_add_i32 s27, s8, s5
	s_add_i32 s26, s27, 4
	s_cmpk_gt_i32 s26, 0x3fff
	s_mov_b64 s[24:25], -1
	s_cbranch_scc0 .LBB0_757
	s_addk_i32 s27, 0xc004
	s_lshr_b32 s42, s27, 8
	s_add_i32 s14, s2, 32
	s_add_i32 s15, s4, 0x200
	v_readlane_b32 s48, v254, 31
	s_and_b32 s14, s14, 0x780
	s_and_b32 s24, s15, 0x700
	s_lshl_b64 s[22:23], s[42:43], 11
	s_lshl_b64 s[20:21], s[42:43], 24
	v_readlane_b32 s60, v254, 43
	v_readlane_b32 s61, v254, 44
	s_add_u32 s20, s60, s20
	s_addc_u32 s21, s61, s21
	s_lshl_b32 s25, s14, 13
	s_add_u32 s20, s20, s25
	s_addc_u32 s21, s21, 0
	s_lshl_b32 s25, s24, 2
	s_add_u32 s20, s20, s25
	v_readlane_b32 s49, v254, 32
	v_readlane_b32 s50, v254, 33
	v_readlane_b32 s51, v254, 34
	v_readlane_b32 s52, v254, 35
	v_readlane_b32 s53, v254, 36
	v_readlane_b32 s54, v254, 37
	v_readlane_b32 s55, v254, 38
	v_readlane_b32 s56, v254, 39
	v_readlane_b32 s57, v254, 40
	v_readlane_b32 s58, v254, 41
	v_readlane_b32 s59, v254, 42
	v_readlane_b32 s62, v254, 45
	v_readlane_b32 s63, v254, 46
	s_mov_b32 s15, s43
	s_addc_u32 s21, s21, 0
	s_or_b32 s22, s22, s24
	s_mov_b64 s[24:25], 0

.LBB0_764:
	s_waitcnt vmcnt(23)
	v_pk_mul_f32 v[44:45], v[44:45], s[98:99]
	v_pk_mul_f32 v[36:37], v[36:37], s[98:99]
	v_cvt_pk_fp8_f32 v1, v44, v36
	v_pk_mul_f32 v[40:41], v[40:41], s[98:99]
	s_waitcnt vmcnt(21)
	v_pk_mul_f32 v[52:53], v[52:53], s[98:99]
	v_cvt_pk_fp8_f32 v1, v40, v52 op_sel:[0,0,1]
	v_cvt_pk_fp8_f32 v135, v45, v37
	v_add_u32_e32 v136, 0x4000, v195
	v_cvt_pk_fp8_f32 v135, v41, v53 op_sel:[0,0,1]
	v_pk_mul_f32 v[42:43], v[42:43], s[98:99]
	v_pk_mul_f32 v[54:55], v[54:55], s[98:99]
	ds_write2_b32 v136, v1, v135 offset0:128 offset1:161
	v_pk_mul_f32 v[46:47], v[46:47], s[98:99]
	v_pk_mul_f32 v[38:39], v[38:39], s[98:99]
	v_cvt_pk_fp8_f32 v1, v46, v38
	s_add_i32 s18, s5, 5
	s_cmp_ge_u32 s18, s71
	v_cvt_pk_fp8_f32 v1, v42, v54 op_sel:[0,0,1]
	v_cvt_pk_fp8_f32 v135, v47, v39
	s_waitcnt vmcnt(18)
	v_pk_mul_f32 v[64:65], v[64:65], s[98:99]
	s_mov_b64 s[18:19], s[10:11]
	v_cvt_pk_fp8_f32 v135, v43, v55 op_sel:[0,0,1]
	ds_write2_b32 v136, v1, v135 offset0:194 offset1:227
	v_pk_mul_f32 v[48:49], v[48:49], s[98:99]
	v_pk_mul_f32 v[56:57], v[56:57], s[98:99]
	v_cvt_pk_fp8_f32 v1, v48, v56
	v_pk_mul_f32 v[60:61], v[60:61], s[98:99]
	v_cvt_pk_fp8_f32 v1, v60, v64 op_sel:[0,0,1]
	v_cvt_pk_fp8_f32 v135, v49, v57
	v_add_u32_e32 v136, 0x6000, v195
	v_cvt_pk_fp8_f32 v135, v61, v65 op_sel:[0,0,1]
	v_pk_mul_f32 v[66:67], v[66:67], s[98:99]
	ds_write2_b32 v136, v1, v135 offset0:192 offset1:225
	v_pk_mul_f32 v[50:51], v[50:51], s[98:99]
	v_pk_mul_f32 v[58:59], v[58:59], s[98:99]
	v_cvt_pk_fp8_f32 v1, v50, v58
	v_pk_mul_f32 v[62:63], v[62:63], s[98:99]
	v_cvt_pk_fp8_f32 v1, v62, v66 op_sel:[0,0,1]
	v_cvt_pk_fp8_f32 v135, v51, v59
	v_add_u32_e32 v136, 0x6400, v195
	v_cvt_pk_fp8_f32 v135, v63, v67 op_sel:[0,0,1]
	ds_write2_b32 v136, v1, v135 offset0:2 offset1:35
	s_cbranch_scc1 .LBB0_771
	s_add_i32 s27, s8, s5
	s_add_i32 s26, s27, 5
	s_cmpk_gt_i32 s26, 0x3fff
	s_mov_b64 s[24:25], -1
	s_cbranch_scc0 .LBB0_767
	s_addk_i32 s27, 0xc005
	s_lshr_b32 s42, s27, 8
	s_add_i32 s18, s2, 40
	s_add_i32 s19, s4, 0x280
	v_readlane_b32 s48, v254, 31
	s_and_b32 s18, s18, 0x780
	s_and_b32 s24, s19, 0x780
	s_lshl_b64 s[22:23], s[42:43], 11
	s_lshl_b64 s[20:21], s[42:43], 24
	v_readlane_b32 s60, v254, 43
	v_readlane_b32 s61, v254, 44
	s_add_u32 s20, s60, s20
	s_addc_u32 s21, s61, s21
	s_lshl_b32 s25, s18, 13
	s_add_u32 s20, s20, s25
	s_addc_u32 s21, s21, 0
	s_lshl_b32 s25, s24, 2
	s_add_u32 s20, s20, s25
	v_readlane_b32 s49, v254, 32
	v_readlane_b32 s50, v254, 33
	v_readlane_b32 s51, v254, 34
	v_readlane_b32 s52, v254, 35
	v_readlane_b32 s53, v254, 36
	v_readlane_b32 s54, v254, 37
	v_readlane_b32 s55, v254, 38
	v_readlane_b32 s56, v254, 39
	v_readlane_b32 s57, v254, 40
	v_readlane_b32 s58, v254, 41
	v_readlane_b32 s59, v254, 42
	v_readlane_b32 s62, v254, 45
	v_readlane_b32 s63, v254, 46
	s_mov_b32 s19, s43
	s_addc_u32 s21, s21, 0
	s_or_b32 s22, s22, s24
	s_mov_b64 s[24:25], 0

.LBB0_772:
	s_waitcnt vmcnt(15)
	v_pk_mul_f32 v[76:77], v[76:77], s[98:99]
	v_pk_mul_f32 v[68:69], v[68:69], s[98:99]
	v_cvt_pk_fp8_f32 v1, v76, v68
	v_pk_mul_f32 v[72:73], v[72:73], s[98:99]
	s_waitcnt vmcnt(13)
	v_pk_mul_f32 v[84:85], v[84:85], s[98:99]
	v_cvt_pk_fp8_f32 v1, v72, v84 op_sel:[0,0,1]
	v_cvt_pk_fp8_f32 v135, v77, v69
	v_pk_mul_f32 v[74:75], v[74:75], s[98:99]
	v_cvt_pk_fp8_f32 v135, v73, v85 op_sel:[0,0,1]
	v_pk_mul_f32 v[86:87], v[86:87], s[98:99]
	s_add_i32 s18, s5, 6
	ds_write2_b32 v195, v1, v135 offset1:33
	v_pk_mul_f32 v[78:79], v[78:79], s[98:99]
	v_pk_mul_f32 v[70:71], v[70:71], s[98:99]
	v_cvt_pk_fp8_f32 v1, v78, v70
	s_cmp_ge_u32 s18, s71
	s_mov_b64 s[18:19], s[0:1]
	v_cvt_pk_fp8_f32 v1, v74, v86 op_sel:[0,0,1]
	v_cvt_pk_fp8_f32 v135, v79, v71
	s_waitcnt vmcnt(11)
	v_pk_mul_f32 v[92:93], v[92:93], s[98:99]
	v_cvt_pk_fp8_f32 v135, v75, v87 op_sel:[0,0,1]
	s_waitcnt vmcnt(10)
	v_pk_mul_f32 v[96:97], v[96:97], s[98:99]
	ds_write2_b32 v195, v1, v135 offset0:66 offset1:99
	v_pk_mul_f32 v[80:81], v[80:81], s[98:99]
	v_pk_mul_f32 v[88:89], v[88:89], s[98:99]
	v_cvt_pk_fp8_f32 v1, v80, v88
	v_cvt_pk_fp8_f32 v1, v92, v96 op_sel:[0,0,1]
	v_cvt_pk_fp8_f32 v135, v81, v89
	v_pk_mul_f32 v[94:95], v[94:95], s[98:99]
	v_cvt_pk_fp8_f32 v135, v93, v97 op_sel:[0,0,1]
	v_pk_mul_f32 v[98:99], v[98:99], s[98:99]
	ds_write2_b32 v134, v1, v135 offset0:64 offset1:97
	v_pk_mul_f32 v[82:83], v[82:83], s[98:99]
	v_pk_mul_f32 v[90:91], v[90:91], s[98:99]
	v_cvt_pk_fp8_f32 v1, v82, v90
	v_cvt_pk_fp8_f32 v1, v94, v98 op_sel:[0,0,1]
	v_cvt_pk_fp8_f32 v135, v83, v91
	v_cvt_pk_fp8_f32 v135, v95, v99 op_sel:[0,0,1]
	ds_write2_b32 v134, v1, v135 offset0:130 offset1:163
	s_cbranch_scc1 .LBB0_779
	s_add_i32 s27, s8, s5
	s_add_i32 s26, s27, 6
	s_cmpk_gt_i32 s26, 0x3fff
	s_mov_b64 s[24:25], -1
	s_cbranch_scc0 .LBB0_775
	s_addk_i32 s27, 0xc006
	s_lshr_b32 s42, s27, 8
	s_add_i32 s18, s2, 48
	s_add_i32 s19, s4, 0x300
	v_readlane_b32 s48, v254, 31
	s_and_b32 s18, s18, 0x780
	s_and_b32 s24, s19, 0x700
	s_lshl_b64 s[22:23], s[42:43], 11
	s_lshl_b64 s[20:21], s[42:43], 24
	v_readlane_b32 s60, v254, 43
	v_readlane_b32 s61, v254, 44
	s_add_u32 s20, s60, s20
	s_addc_u32 s21, s61, s21
	s_lshl_b32 s25, s18, 13
	s_add_u32 s20, s20, s25
	s_addc_u32 s21, s21, 0
	s_lshl_b32 s25, s24, 2
	s_add_u32 s20, s20, s25
	v_readlane_b32 s49, v254, 32
	v_readlane_b32 s50, v254, 33
	v_readlane_b32 s51, v254, 34
	v_readlane_b32 s52, v254, 35
	v_readlane_b32 s53, v254, 36
	v_readlane_b32 s54, v254, 37
	v_readlane_b32 s55, v254, 38
	v_readlane_b32 s56, v254, 39
	v_readlane_b32 s57, v254, 40
	v_readlane_b32 s58, v254, 41
	v_readlane_b32 s59, v254, 42
	v_readlane_b32 s62, v254, 45
	v_readlane_b32 s63, v254, 46
	s_mov_b32 s19, s43
	s_addc_u32 s21, s21, 0
	s_or_b32 s22, s22, s24
	s_mov_b64 s[24:25], 0

.LBB0_780:
	s_waitcnt vmcnt(7)
	v_pk_mul_f32 v[108:109], v[108:109], s[98:99]
	v_pk_mul_f32 v[100:101], v[100:101], s[98:99]
	v_cvt_pk_fp8_f32 v1, v108, v100
	v_pk_mul_f32 v[104:105], v[104:105], s[98:99]
	s_waitcnt vmcnt(5)
	v_pk_mul_f32 v[116:117], v[116:117], s[98:99]
	v_cvt_pk_fp8_f32 v1, v104, v116 op_sel:[0,0,1]
	v_cvt_pk_fp8_f32 v134, v109, v101
	v_add_u32_e32 v135, 0x4000, v195
	v_cvt_pk_fp8_f32 v134, v105, v117 op_sel:[0,0,1]
	v_pk_mul_f32 v[106:107], v[106:107], s[98:99]
	v_pk_mul_f32 v[118:119], v[118:119], s[98:99]
	ds_write2_b32 v135, v1, v134 offset0:128 offset1:161
	v_pk_mul_f32 v[110:111], v[110:111], s[98:99]
	v_pk_mul_f32 v[102:103], v[102:103], s[98:99]
	v_cvt_pk_fp8_f32 v1, v110, v102
	s_add_i32 s18, s5, 7
	s_cmp_ge_u32 s18, s71
	v_cvt_pk_fp8_f32 v1, v106, v118 op_sel:[0,0,1]
	v_cvt_pk_fp8_f32 v134, v111, v103
	s_waitcnt vmcnt(2)
	v_pk_mul_f32 v[128:129], v[128:129], s[98:99]
	s_mov_b64 s[18:19], s[12:13]
	v_cvt_pk_fp8_f32 v134, v107, v119 op_sel:[0,0,1]
	ds_write2_b32 v135, v1, v134 offset0:194 offset1:227
	v_pk_mul_f32 v[112:113], v[112:113], s[98:99]
	v_pk_mul_f32 v[120:121], v[120:121], s[98:99]
	v_cvt_pk_fp8_f32 v1, v112, v120
	v_pk_mul_f32 v[124:125], v[124:125], s[98:99]
	v_cvt_pk_fp8_f32 v1, v124, v128 op_sel:[0,0,1]
	v_cvt_pk_fp8_f32 v134, v113, v121
	v_add_u32_e32 v135, 0x6000, v195
	v_cvt_pk_fp8_f32 v134, v125, v129 op_sel:[0,0,1]
	v_pk_mul_f32 v[130:131], v[130:131], s[98:99]
	ds_write2_b32 v135, v1, v134 offset0:192 offset1:225
	v_pk_mul_f32 v[114:115], v[114:115], s[98:99]
	v_pk_mul_f32 v[122:123], v[122:123], s[98:99]
	v_cvt_pk_fp8_f32 v1, v114, v122
	v_pk_mul_f32 v[126:127], v[126:127], s[98:99]
	v_cvt_pk_fp8_f32 v1, v126, v130 op_sel:[0,0,1]
	v_cvt_pk_fp8_f32 v134, v115, v123
	v_add_u32_e32 v135, 0x6400, v195
	v_cvt_pk_fp8_f32 v134, v127, v131 op_sel:[0,0,1]
	ds_write2_b32 v135, v1, v134 offset0:2 offset1:35
	s_cbranch_scc1 .LBB0_752
	s_add_i32 s26, s8, s5
	s_add_i32 s5, s26, 7
	s_cmpk_gt_i32 s5, 0x3fff
	s_mov_b64 s[24:25], -1
	s_cbranch_scc0 .LBB0_783
	s_addk_i32 s26, 0xc007
	s_lshr_b32 s42, s26, 8
	s_add_i32 s18, s2, 56
	s_add_i32 s19, s4, 0x380
	v_readlane_b32 s48, v254, 31
	s_and_b32 s18, s18, 0x780
	s_and_b32 s24, s19, 0x780
	s_lshl_b64 s[22:23], s[42:43], 11
	s_lshl_b64 s[20:21], s[42:43], 24
	v_readlane_b32 s60, v254, 43
	v_readlane_b32 s61, v254, 44
	s_add_u32 s20, s60, s20
	s_addc_u32 s21, s61, s21
	s_lshl_b32 s25, s18, 13
	s_add_u32 s20, s20, s25
	s_addc_u32 s21, s21, 0
	s_lshl_b32 s25, s24, 2
	s_add_u32 s20, s20, s25
	v_readlane_b32 s49, v254, 32
	v_readlane_b32 s50, v254, 33
	v_readlane_b32 s51, v254, 34
	v_readlane_b32 s52, v254, 35
	v_readlane_b32 s53, v254, 36
	v_readlane_b32 s54, v254, 37
	v_readlane_b32 s55, v254, 38
	v_readlane_b32 s56, v254, 39
	v_readlane_b32 s57, v254, 40
	v_readlane_b32 s58, v254, 41
	v_readlane_b32 s59, v254, 42
	v_readlane_b32 s62, v254, 45
	v_readlane_b32 s63, v254, 46
	s_mov_b32 s19, s43
	s_addc_u32 s21, s21, 0
	s_or_b32 s22, s22, s24
	s_mov_b64 s[24:25], 0

.LBB0_923:
	v_mul_lo_u32 v143, v221, s41
	v_lshl_add_u32 v143, v206, 1, v143
	v_add_u32_e32 v143, 0x2000, v143
	s_mov_b64 s[98:99], s[12:13]
	global_load_dwordx4 v[144:147], v143, s[98:99]
	global_load_dwordx4 v[148:151], v143, s[98:99] offset:256
	s_add_u32 s98, s98, 0x68800
	s_addc_u32 s99, s99, 0
	global_load_dwordx4 v[152:155], v143, s[98:99]
	global_load_dwordx4 v[156:159], v143, s[98:99] offset:256
	s_add_u32 s98, s98, 0x68800
	s_addc_u32 s99, s99, 0
	global_load_dwordx4 v[160:163], v143, s[98:99]
	global_load_dwordx4 v[164:167], v143, s[98:99] offset:256
	s_add_u32 s98, s98, 0x68800
	s_addc_u32 s99, s99, 0
	global_load_dwordx4 v[168:171], v143, s[98:99]
	global_load_dwordx4 v[172:175], v143, s[98:99] offset:256
	s_add_u32 s98, s98, 0x20a800
	s_addc_u32 s99, s99, 0
	global_load_dwordx4 v[176:179], v143, s[98:99]
	global_load_dwordx4 v[180:183], v143, s[98:99] offset:256
	s_add_u32 s98, s98, 0x68800
	s_addc_u32 s99, s99, 0
	global_load_dwordx4 v[184:187], v143, s[98:99]
	global_load_dwordx4 v[188:191], v143, s[98:99] offset:256
	s_add_u32 s98, s98, 0x68800
	s_addc_u32 s99, s99, 0
	global_load_dwordx4 v[222:225], v143, s[98:99]
	global_load_dwordx4 v[226:229], v143, s[98:99] offset:256
	s_add_u32 s98, s98, 0x68800
	s_addc_u32 s99, s99, 0
	global_load_dwordx4 v[230:233], v143, s[98:99]
	global_load_dwordx4 v[234:237], v143, s[98:99] offset:256
	v_mov_b64_e32 v[132:133], s[12:13]
	v_mad_i64_i32 v[134:135], s[22:23], v221, s41, v[132:133]
	v_lshlrev_b64 v[130:131], 1, v[206:207]
	v_lshl_add_u64 v[134:135], v[134:135], 0, v[130:131]
	v_add_co_u32_e32 v138, vcc, 0x2000, v134
	s_nop 1
	v_addc_co_u32_e32 v139, vcc, 0, v135, vcc
	s_waitcnt vmcnt(15)
	v_lshlrev_b32_e32 v1, 16, v144
	v_and_b32_e32 v134, 0xffff0000, v144
	v_lshlrev_b32_e32 v140, 16, v145
	v_lshlrev_b32_e32 v142, 16, v147
	v_and_b32_e32 v137, 0xffff0000, v147
	v_and_b32_e32 v135, 0xffff0000, v145
	v_lshlrev_b32_e32 v141, 16, v146
	v_and_b32_e32 v136, 0xffff0000, v146
	v_mul_f32_e32 v1, v126, v1
	v_mul_f32_e32 v126, v127, v134
	v_mul_f32_e32 v127, v128, v140
	v_mul_f32_e32 v134, v125, v137
	v_mul_f32_e32 v128, v129, v135
	v_mul_f32_e32 v122, v122, v141
	v_mul_f32_e32 v123, v123, v136
	v_mul_f32_e32 v129, v124, v142
	v_cvt_pk_bf16_f32 v124, v1, v126
	v_cvt_pk_bf16_f32 v125, v127, v128
	v_cvt_pk_bf16_f32 v126, v122, v123
	v_cvt_pk_bf16_f32 v127, v129, v134
	v_mov_b64_e32 v[122:123], s[4:5]
	v_or_b32_e32 v1, 16, v221
	v_mad_i64_i32 v[128:129], s[22:23], v221, s46, v[122:123]
	v_mad_i64_i32 v[138:139], s[22:23], v1, s41, v[132:133]
	v_lshl_add_u64 v[128:129], v[128:129], 0, v[130:131]
	v_lshl_add_u64 v[138:139], v[138:139], 0, v[130:131]
	v_add_co_u32_e32 v138, vcc, s39, v138
	global_store_dwordx4 v[128:129], v[124:127], off
	s_nop 0
	v_addc_co_u32_e32 v139, vcc, 0, v139, vcc
	s_waitcnt vmcnt(15)
	v_lshlrev_b32_e32 v124, 16, v148
	v_and_b32_e32 v125, 0xffff0000, v148
	v_lshlrev_b32_e32 v126, 16, v149
	v_and_b32_e32 v127, 0xffff0000, v149
	v_lshlrev_b32_e32 v134, 16, v150
	v_and_b32_e32 v135, 0xffff0000, v150
	v_lshlrev_b32_e32 v136, 16, v151
	v_and_b32_e32 v137, 0xffff0000, v151
	v_mul_f32_e32 v118, v118, v124
	v_mul_f32_e32 v119, v119, v125
	v_mul_f32_e32 v120, v120, v126
	v_mul_f32_e32 v121, v121, v127
	v_mul_f32_e32 v113, v113, v137
	v_mul_f32_e32 v124, v110, v134
	v_mul_f32_e32 v125, v111, v135
	v_mul_f32_e32 v126, v112, v136
	v_cvt_pk_bf16_f32 v110, v118, v119
	v_cvt_pk_bf16_f32 v111, v120, v121
	v_cvt_pk_bf16_f32 v112, v124, v125
	v_cvt_pk_bf16_f32 v113, v126, v113
	s_nop 0
	global_store_dwordx4 v[128:129], v[110:113], off offset:256
	s_waitcnt vmcnt(15)
	s_nop 0
	v_lshlrev_b32_e32 v110, 16, v152
	v_and_b32_e32 v111, 0xffff0000, v152
	v_lshlrev_b32_e32 v112, 16, v153
	v_and_b32_e32 v113, 0xffff0000, v153
	v_lshlrev_b32_e32 v118, 16, v154
	v_and_b32_e32 v119, 0xffff0000, v154
	v_lshlrev_b32_e32 v120, 16, v155
	v_and_b32_e32 v121, 0xffff0000, v155
	v_mul_f32_e32 v110, v114, v110
	v_mul_f32_e32 v111, v115, v111
	v_mul_f32_e32 v112, v116, v112
	v_mul_f32_e32 v113, v117, v113
	v_mul_f32_e32 v109, v109, v121
	v_mul_f32_e32 v114, v106, v118
	v_mul_f32_e32 v115, v107, v119
	v_mul_f32_e32 v116, v108, v120
	v_cvt_pk_bf16_f32 v106, v110, v111
	v_cvt_pk_bf16_f32 v107, v112, v113
	v_cvt_pk_bf16_f32 v108, v114, v115
	v_cvt_pk_bf16_f32 v109, v116, v109
	v_or_b32_e32 v118, 32, v221
	v_mad_i64_i32 v[114:115], s[22:23], v1, s46, v[122:123]
	v_mad_i64_i32 v[116:117], s[22:23], v118, s41, v[132:133]
	v_lshl_add_u64 v[114:115], v[114:115], 0, v[130:131]
	v_lshl_add_u64 v[116:117], v[116:117], 0, v[130:131]
	v_add_co_u32_e32 v116, vcc, s39, v116
	global_store_dwordx4 v[114:115], v[106:109], off
	s_nop 0
	v_addc_co_u32_e32 v117, vcc, 0, v117, vcc
	s_waitcnt vmcnt(15)
	v_lshlrev_b32_e32 v1, 16, v156
	v_and_b32_e32 v106, 0xffff0000, v156
	v_lshlrev_b32_e32 v107, 16, v157
	v_and_b32_e32 v108, 0xffff0000, v157
	v_lshlrev_b32_e32 v109, 16, v158
	v_and_b32_e32 v110, 0xffff0000, v158
	v_and_b32_e32 v112, 0xffff0000, v159
	v_lshlrev_b32_e32 v111, 16, v159
	v_mul_f32_e32 v1, v102, v1
	v_mul_f32_e32 v102, v103, v106
	v_mul_f32_e32 v103, v104, v107
	v_mul_f32_e32 v104, v105, v108
	v_mul_f32_e32 v105, v94, v109
	v_mul_f32_e32 v97, v97, v112
	v_mul_f32_e32 v106, v95, v110
	v_mul_f32_e32 v107, v96, v111
	v_cvt_pk_bf16_f32 v94, v1, v102
	v_cvt_pk_bf16_f32 v95, v103, v104
	v_cvt_pk_bf16_f32 v96, v105, v106
	v_cvt_pk_bf16_f32 v97, v107, v97
	s_waitcnt vmcnt(15)
	v_lshlrev_b32_e32 v1, 16, v160
	global_store_dwordx4 v[114:115], v[94:97], off offset:256
	v_mul_f32_e32 v1, v98, v1
	s_nop 0
	v_and_b32_e32 v94, 0xffff0000, v160
	v_lshlrev_b32_e32 v95, 16, v161
	v_and_b32_e32 v96, 0xffff0000, v161
	v_lshlrev_b32_e32 v97, 16, v162
	v_and_b32_e32 v102, 0xffff0000, v162
	v_and_b32_e32 v104, 0xffff0000, v163
	v_lshlrev_b32_e32 v103, 16, v163
	v_mul_f32_e32 v94, v99, v94
	v_mul_f32_e32 v95, v100, v95
	v_mul_f32_e32 v96, v101, v96
	v_mul_f32_e32 v97, v90, v97
	v_mul_f32_e32 v93, v93, v104
	v_mul_f32_e32 v98, v91, v102
	v_mul_f32_e32 v99, v92, v103
	v_cvt_pk_bf16_f32 v90, v1, v94
	v_cvt_pk_bf16_f32 v91, v95, v96
	v_cvt_pk_bf16_f32 v92, v97, v98
	v_cvt_pk_bf16_f32 v93, v99, v93
	v_or_b32_e32 v1, 48, v221
	v_mad_i64_i32 v[98:99], s[22:23], v118, s46, v[122:123]
	v_mad_i64_i32 v[100:101], s[22:23], v1, s41, v[132:133]
	v_lshl_add_u64 v[98:99], v[98:99], 0, v[130:131]
	v_lshl_add_u64 v[100:101], v[100:101], 0, v[130:131]
	v_add_co_u32_e32 v100, vcc, s39, v100
	global_store_dwordx4 v[98:99], v[90:93], off
	s_nop 0
	v_addc_co_u32_e32 v101, vcc, 0, v101, vcc
	s_waitcnt vmcnt(15)
	v_lshlrev_b32_e32 v90, 16, v164
	v_and_b32_e32 v91, 0xffff0000, v164
	v_lshlrev_b32_e32 v92, 16, v165
	v_and_b32_e32 v93, 0xffff0000, v165
	v_lshlrev_b32_e32 v94, 16, v166
	v_and_b32_e32 v95, 0xffff0000, v166
	v_lshlrev_b32_e32 v96, 16, v167
	v_and_b32_e32 v97, 0xffff0000, v167
	v_mul_f32_e32 v86, v86, v90
	v_mul_f32_e32 v87, v87, v91
	v_mul_f32_e32 v88, v88, v92
	v_mul_f32_e32 v89, v89, v93
	v_mul_f32_e32 v81, v81, v97
	v_mul_f32_e32 v90, v78, v94
	v_mul_f32_e32 v91, v79, v95
	v_mul_f32_e32 v92, v80, v96
	v_cvt_pk_bf16_f32 v78, v86, v87
	v_cvt_pk_bf16_f32 v79, v88, v89
	v_cvt_pk_bf16_f32 v80, v90, v91
	v_cvt_pk_bf16_f32 v81, v92, v81
	s_nop 0
	global_store_dwordx4 v[98:99], v[78:81], off offset:256
	s_waitcnt vmcnt(15)
	s_nop 0
	v_lshlrev_b32_e32 v78, 16, v168
	v_and_b32_e32 v79, 0xffff0000, v168
	v_lshlrev_b32_e32 v80, 16, v169
	v_and_b32_e32 v81, 0xffff0000, v169
	v_lshlrev_b32_e32 v86, 16, v170
	v_and_b32_e32 v87, 0xffff0000, v170
	v_lshlrev_b32_e32 v88, 16, v171
	v_and_b32_e32 v89, 0xffff0000, v171
	v_mul_f32_e32 v78, v82, v78
	v_mul_f32_e32 v79, v83, v79
	v_mul_f32_e32 v80, v84, v80
	v_mul_f32_e32 v81, v85, v81
	v_mul_f32_e32 v77, v77, v89
	v_mul_f32_e32 v82, v74, v86
	v_mul_f32_e32 v83, v75, v87
	v_mul_f32_e32 v84, v76, v88
	v_cvt_pk_bf16_f32 v74, v78, v79
	v_cvt_pk_bf16_f32 v75, v80, v81
	v_cvt_pk_bf16_f32 v76, v82, v83
	v_cvt_pk_bf16_f32 v77, v84, v77
	v_add_u32_e32 v86, 0x80, v221
	v_mad_i64_i32 v[82:83], s[22:23], v1, s46, v[122:123]
	v_mad_i64_i32 v[84:85], s[22:23], v86, s41, v[132:133]
	v_lshl_add_u64 v[82:83], v[82:83], 0, v[130:131]
	v_lshl_add_u64 v[84:85], v[84:85], 0, v[130:131]
	v_add_co_u32_e32 v84, vcc, s39, v84
	global_store_dwordx4 v[82:83], v[74:77], off
	s_nop 0
	v_addc_co_u32_e32 v85, vcc, 0, v85, vcc
	s_waitcnt vmcnt(15)
	v_lshlrev_b32_e32 v1, 16, v172
	v_and_b32_e32 v74, 0xffff0000, v172
	v_lshlrev_b32_e32 v75, 16, v173
	v_and_b32_e32 v76, 0xffff0000, v173
	v_lshlrev_b32_e32 v77, 16, v174
	v_and_b32_e32 v78, 0xffff0000, v174
	v_and_b32_e32 v80, 0xffff0000, v175
	v_lshlrev_b32_e32 v79, 16, v175
	v_mul_f32_e32 v1, v70, v1
	v_mul_f32_e32 v70, v71, v74
	v_mul_f32_e32 v71, v72, v75
	v_mul_f32_e32 v72, v73, v76
	v_mul_f32_e32 v73, v66, v77
	v_mul_f32_e32 v69, v69, v80
	v_mul_f32_e32 v74, v67, v78
	v_mul_f32_e32 v75, v68, v79
	v_cvt_pk_bf16_f32 v66, v1, v70
	v_cvt_pk_bf16_f32 v67, v71, v72
	v_cvt_pk_bf16_f32 v68, v73, v74
	v_cvt_pk_bf16_f32 v69, v75, v69
	s_waitcnt vmcnt(15)
	v_lshlrev_b32_e32 v1, 16, v176
	global_store_dwordx4 v[82:83], v[66:69], off offset:256
	v_mul_f32_e32 v1, v62, v1
	s_nop 0
	v_and_b32_e32 v66, 0xffff0000, v176
	v_lshlrev_b32_e32 v67, 16, v177
	v_and_b32_e32 v68, 0xffff0000, v177
	v_lshlrev_b32_e32 v69, 16, v178
	v_and_b32_e32 v70, 0xffff0000, v178
	v_and_b32_e32 v72, 0xffff0000, v179
	v_lshlrev_b32_e32 v71, 16, v179
	v_mul_f32_e32 v62, v63, v66
	v_mul_f32_e32 v63, v64, v67
	v_mul_f32_e32 v64, v65, v68
	v_mul_f32_e32 v65, v58, v69
	v_mul_f32_e32 v61, v61, v72
	v_mul_f32_e32 v66, v59, v70
	v_mul_f32_e32 v67, v60, v71
	v_cvt_pk_bf16_f32 v58, v1, v62
	v_cvt_pk_bf16_f32 v59, v63, v64
	v_cvt_pk_bf16_f32 v60, v65, v66
	v_cvt_pk_bf16_f32 v61, v67, v61
	v_add_u32_e32 v1, 0x90, v221
	v_mad_i64_i32 v[66:67], s[22:23], v86, s46, v[122:123]
	v_mad_i64_i32 v[68:69], s[22:23], v1, s41, v[132:133]
	v_lshl_add_u64 v[66:67], v[66:67], 0, v[130:131]
	v_lshl_add_u64 v[68:69], v[68:69], 0, v[130:131]
	v_add_co_u32_e32 v68, vcc, s39, v68
	global_store_dwordx4 v[66:67], v[58:61], off
	s_nop 0
	v_addc_co_u32_e32 v69, vcc, 0, v69, vcc
	s_waitcnt vmcnt(15)
	v_lshlrev_b32_e32 v58, 16, v180
	v_and_b32_e32 v59, 0xffff0000, v180
	v_lshlrev_b32_e32 v60, 16, v181
	v_and_b32_e32 v61, 0xffff0000, v181
	v_lshlrev_b32_e32 v62, 16, v182
	v_and_b32_e32 v63, 0xffff0000, v182
	v_lshlrev_b32_e32 v64, 16, v183
	v_and_b32_e32 v65, 0xffff0000, v183
	v_mul_f32_e32 v54, v54, v58
	v_mul_f32_e32 v55, v55, v59
	v_mul_f32_e32 v56, v56, v60
	v_mul_f32_e32 v57, v57, v61
	v_mul_f32_e32 v49, v49, v65
	v_mul_f32_e32 v58, v46, v62
	v_mul_f32_e32 v59, v47, v63
	v_mul_f32_e32 v60, v48, v64
	v_cvt_pk_bf16_f32 v46, v54, v55
	v_cvt_pk_bf16_f32 v47, v56, v57
	v_cvt_pk_bf16_f32 v48, v58, v59
	v_cvt_pk_bf16_f32 v49, v60, v49
	s_nop 0
	global_store_dwordx4 v[66:67], v[46:49], off offset:256
	s_waitcnt vmcnt(15)
	s_nop 0
	v_lshlrev_b32_e32 v46, 16, v184
	v_and_b32_e32 v47, 0xffff0000, v184
	v_lshlrev_b32_e32 v48, 16, v185
	v_and_b32_e32 v49, 0xffff0000, v185
	v_lshlrev_b32_e32 v54, 16, v186
	v_and_b32_e32 v55, 0xffff0000, v186
	v_lshlrev_b32_e32 v56, 16, v187
	v_and_b32_e32 v57, 0xffff0000, v187
	v_mul_f32_e32 v46, v50, v46
	v_mul_f32_e32 v47, v51, v47
	v_mul_f32_e32 v48, v52, v48
	v_mul_f32_e32 v49, v53, v49
	v_mul_f32_e32 v45, v45, v57
	v_mul_f32_e32 v50, v42, v54
	v_mul_f32_e32 v51, v43, v55
	v_mul_f32_e32 v52, v44, v56
	v_cvt_pk_bf16_f32 v42, v46, v47
	v_cvt_pk_bf16_f32 v43, v48, v49
	v_cvt_pk_bf16_f32 v44, v50, v51
	v_cvt_pk_bf16_f32 v45, v52, v45
	v_add_u32_e32 v54, 0xa0, v221
	v_mad_i64_i32 v[50:51], s[22:23], v1, s46, v[122:123]
	v_mad_i64_i32 v[52:53], s[22:23], v54, s41, v[132:133]
	v_lshl_add_u64 v[50:51], v[50:51], 0, v[130:131]
	v_lshl_add_u64 v[52:53], v[52:53], 0, v[130:131]
	v_add_co_u32_e32 v52, vcc, s39, v52
	global_store_dwordx4 v[50:51], v[42:45], off
	s_nop 0
	v_addc_co_u32_e32 v53, vcc, 0, v53, vcc
	s_waitcnt vmcnt(15)
	v_lshlrev_b32_e32 v1, 16, v188
	v_and_b32_e32 v42, 0xffff0000, v188
	v_lshlrev_b32_e32 v43, 16, v189
	v_and_b32_e32 v44, 0xffff0000, v189
	v_lshlrev_b32_e32 v45, 16, v190
	v_and_b32_e32 v46, 0xffff0000, v190
	v_and_b32_e32 v48, 0xffff0000, v191
	v_lshlrev_b32_e32 v47, 16, v191
	v_mul_f32_e32 v1, v38, v1
	v_mul_f32_e32 v38, v39, v42
	v_mul_f32_e32 v39, v40, v43
	v_mul_f32_e32 v40, v41, v44
	v_mul_f32_e32 v41, v30, v45
	v_mul_f32_e32 v33, v33, v48
	v_mul_f32_e32 v42, v31, v46
	v_mul_f32_e32 v43, v32, v47
	v_cvt_pk_bf16_f32 v30, v1, v38
	v_cvt_pk_bf16_f32 v31, v39, v40
	v_cvt_pk_bf16_f32 v32, v41, v42
	v_cvt_pk_bf16_f32 v33, v43, v33
	s_waitcnt vmcnt(15)
	v_lshlrev_b32_e32 v1, 16, v222
	global_store_dwordx4 v[50:51], v[30:33], off offset:256
	v_mul_f32_e32 v1, v34, v1
	s_nop 0
	v_and_b32_e32 v30, 0xffff0000, v222
	v_lshlrev_b32_e32 v31, 16, v223
	v_and_b32_e32 v32, 0xffff0000, v223
	v_lshlrev_b32_e32 v33, 16, v224
	v_and_b32_e32 v38, 0xffff0000, v224
	v_and_b32_e32 v40, 0xffff0000, v225
	v_lshlrev_b32_e32 v39, 16, v225
	v_mul_f32_e32 v30, v35, v30
	v_mul_f32_e32 v31, v36, v31
	v_mul_f32_e32 v32, v37, v32
	v_mul_f32_e32 v33, v26, v33
	v_mul_f32_e32 v29, v29, v40
	v_mul_f32_e32 v34, v27, v38
	v_mul_f32_e32 v35, v28, v39
	v_cvt_pk_bf16_f32 v26, v1, v30
	v_cvt_pk_bf16_f32 v27, v31, v32
	v_cvt_pk_bf16_f32 v28, v33, v34
	v_cvt_pk_bf16_f32 v29, v35, v29
	v_add_u32_e32 v1, 0xb0, v221
	v_mad_i64_i32 v[34:35], s[22:23], v54, s46, v[122:123]
	v_mad_i64_i32 v[36:37], s[22:23], v1, s41, v[132:133]
	v_lshl_add_u64 v[34:35], v[34:35], 0, v[130:131]
	v_lshl_add_u64 v[36:37], v[36:37], 0, v[130:131]
	v_add_co_u32_e32 v36, vcc, s39, v36
	global_store_dwordx4 v[34:35], v[26:29], off
	s_nop 0
	v_addc_co_u32_e32 v37, vcc, 0, v37, vcc
	s_and_b64 vcc, exec, s[0:1]
	s_waitcnt vmcnt(15)
	v_lshlrev_b32_e32 v26, 16, v226
	v_and_b32_e32 v27, 0xffff0000, v226
	v_lshlrev_b32_e32 v28, 16, v227
	v_and_b32_e32 v29, 0xffff0000, v227
	v_lshlrev_b32_e32 v30, 16, v228
	v_and_b32_e32 v31, 0xffff0000, v228
	v_lshlrev_b32_e32 v32, 16, v229
	v_and_b32_e32 v33, 0xffff0000, v229
	v_mul_f32_e32 v22, v22, v26
	v_mul_f32_e32 v23, v23, v27
	v_mul_f32_e32 v24, v24, v28
	v_mul_f32_e32 v25, v25, v29
	v_mul_f32_e32 v17, v17, v33
	v_mul_f32_e32 v26, v14, v30
	v_mul_f32_e32 v27, v15, v31
	v_mul_f32_e32 v28, v16, v32
	v_cvt_pk_bf16_f32 v14, v22, v23
	v_cvt_pk_bf16_f32 v15, v24, v25
	v_cvt_pk_bf16_f32 v16, v26, v27
	v_cvt_pk_bf16_f32 v17, v28, v17
	s_nop 0
	global_store_dwordx4 v[34:35], v[14:17], off offset:256
	s_waitcnt vmcnt(15)
	s_nop 0
	v_lshlrev_b32_e32 v14, 16, v230
	v_and_b32_e32 v15, 0xffff0000, v230
	v_lshlrev_b32_e32 v16, 16, v231
	v_and_b32_e32 v17, 0xffff0000, v231
	v_lshlrev_b32_e32 v22, 16, v232
	v_and_b32_e32 v23, 0xffff0000, v232
	v_lshlrev_b32_e32 v24, 16, v233
	v_and_b32_e32 v25, 0xffff0000, v233
	v_mul_f32_e32 v14, v18, v14
	v_mul_f32_e32 v15, v19, v15
	v_mul_f32_e32 v16, v20, v16
	v_mul_f32_e32 v17, v21, v17
	v_mul_f32_e32 v13, v13, v25
	v_mul_f32_e32 v18, v10, v22
	v_mul_f32_e32 v19, v11, v23
	v_mul_f32_e32 v20, v12, v24
	v_cvt_pk_bf16_f32 v10, v14, v15
	v_cvt_pk_bf16_f32 v11, v16, v17
	v_cvt_pk_bf16_f32 v12, v18, v19
	v_cvt_pk_bf16_f32 v13, v20, v13
	v_mad_i64_i32 v[18:19], s[22:23], v1, s46, v[122:123]
	v_lshl_add_u64 v[18:19], v[18:19], 0, v[130:131]
	global_store_dwordx4 v[18:19], v[10:13], off
	s_waitcnt vmcnt(15)
	v_lshlrev_b32_e32 v1, 16, v234
	v_and_b32_e32 v10, 0xffff0000, v234
	v_lshlrev_b32_e32 v13, 16, v236
	v_and_b32_e32 v14, 0xffff0000, v236
	v_and_b32_e32 v16, 0xffff0000, v237
	v_lshlrev_b32_e32 v11, 16, v235
	v_and_b32_e32 v12, 0xffff0000, v235
	v_lshlrev_b32_e32 v15, 16, v237
	v_mul_f32_e32 v5, v5, v16
	v_mul_f32_e32 v1, v6, v1
	v_mul_f32_e32 v6, v7, v10
	v_mul_f32_e32 v7, v8, v11
	v_mul_f32_e32 v8, v9, v12
	v_mul_f32_e32 v9, v2, v13
	v_mul_f32_e32 v10, v3, v14
	v_mul_f32_e32 v11, v4, v15
	v_cvt_pk_bf16_f32 v2, v1, v6
	v_cvt_pk_bf16_f32 v3, v7, v8
	v_cvt_pk_bf16_f32 v4, v9, v10
	v_cvt_pk_bf16_f32 v5, v11, v5
	global_store_dwordx4 v[18:19], v[2:5], off offset:256
	s_cbranch_vccnz .LBB0_926
	s_andn2_b64 vcc, exec, s[10:11]
	s_cbranch_vccnz .LBB0_903
	s_barrier
	s_branch .LBB0_903
